# indexer scoring as compact LDS-staged loop + grid-barrier L1 invalidate issued early
# speedup vs baseline: 1.0061x; 1.0061x over previous
.LBB0_307:
	s_lshl_b32 s24, s33, 6
	s_add_i32 s6, s24, 0x500
	s_mov_b32 s7, 0
	s_lshl_b64 s[4:5], s[6:7], 2
	s_add_u32 s4, s36, s4
	s_addc_u32 s5, s37, s5
	v_mov_b32_e32 v1, 1
	v_mov_b64_e32 v[6:7], s[4:5]
	flat_atomic_add v1, v[6:7], v1 sc0
	v_cvt_f32_u32_e32 v3, v4
	v_sub_u32_e32 v5, 0, v4
	v_rcp_iflag_f32_e32 v3, v3
	s_nop 0
	v_mul_f32_e32 v3, 0x4f7ffffe, v3
	v_cvt_u32_f32_e32 v3, v3
	v_mul_lo_u32 v5, v5, v3
	v_mul_hi_u32 v5, v3, v5
	v_add_u32_e32 v3, v3, v5
	s_waitcnt vmcnt(0) lgkmcnt(0)
	buffer_inv sc1
	v_mul_hi_u32 v3, v1, v3
	v_mul_lo_u32 v5, v3, v4
	v_add_u32_e32 v6, 1, v1
	v_sub_u32_e32 v1, v1, v5
	v_add_u32_e32 v7, 1, v3
	v_cmp_ge_u32_e32 vcc, v1, v4
	v_sub_u32_e32 v5, v1, v4
	s_nop 0
	v_cndmask_b32_e32 v3, v3, v7, vcc
	v_cndmask_b32_e32 v1, v1, v5, vcc
	v_add_u32_e32 v5, 1, v3
	v_cmp_ge_u32_e32 vcc, v1, v4
	s_nop 1
	v_cndmask_b32_e32 v1, v3, v5, vcc
	v_mad_u64_u32 v[4:5], s[4:5], v4, v1, v[4:5]
	v_cmp_ne_u32_e32 vcc, v6, v4
	s_and_saveexec_b64 s[4:5], vcc
	s_xor_b64 s[4:5], exec, s[4:5]
	s_cbranch_execz .LBB0_320
	s_add_i32 s6, s24, 0x900
	s_lshl_b64 s[6:7], s[6:7], 2
	s_add_u32 s8, s36, s6
	s_addc_u32 s9, s37, s7
	v_mov_b64_e32 v[2:3], s[8:9]
	flat_load_dword v2, v[2:3] sc1
	s_waitcnt vmcnt(0) lgkmcnt(0)
	v_cmp_eq_u32_e32 vcc, v2, v1
	s_and_saveexec_b64 s[6:7], vcc
	s_cbranch_execz .LBB0_319
	s_mov_b32 s25, 1
	s_mov_b64 s[10:11], 0
	s_branch .LBB0_311

.LBB0_319:
	s_or_b64 exec, exec, s[6:7]
	s_waitcnt vmcnt(0) lgkmcnt(0)
	s_waitcnt vmcnt(0)

.LBB0_335:
	s_or_b64 exec, exec, s[4:5]
	s_add_i32 s4, s24, 0x900
	s_mov_b32 s5, 0
	s_lshl_b64 s[4:5], s[4:5], 2
	s_add_u32 s4, s36, s4
	s_addc_u32 s5, s37, s5
	v_mov_b32_e32 v1, 1
	v_mov_b64_e32 v[2:3], s[4:5]
	s_waitcnt vmcnt(0) lgkmcnt(0)
	flat_atomic_add v[2:3], v1
	s_waitcnt vmcnt(0)

.LBB0_340:
	s_or_b64 exec, exec, s[10:11]
	s_add_i32 s48, s30, 0x900
	s_lshl_b64 s[10:11], s[48:49], 2
	s_add_u32 s6, s6, s10
	s_addc_u32 s7, s7, s11
	v_mov_b64_e32 v[4:5], s[6:7]
	s_waitcnt vmcnt(0) lgkmcnt(0)
	flat_atomic_add v[4:5], v232
	s_waitcnt vmcnt(0)

.LBB0_345:
	s_or_b64 exec, exec, s[6:7]
	s_add_i32 s48, s28, 0x900
	s_lshl_b64 s[6:7], s[48:49], 2
	s_add_u32 s4, s4, s6
	s_addc_u32 s5, s5, s7
	v_mov_b64_e32 v[4:5], s[4:5]
	s_waitcnt vmcnt(0) lgkmcnt(0)
	flat_atomic_add v[4:5], v232
	s_waitcnt vmcnt(0)

.LBB0_577:
	s_lshl_b32 s30, s42, 6
	s_add_i32 s48, s30, 0x500
	s_lshl_b64 s[10:11], s[48:49], 2
	s_add_u32 s10, s6, s10
	s_addc_u32 s11, s7, s11
	v_mov_b64_e32 v[6:7], s[10:11]
	flat_atomic_add v6, v[6:7], v232 sc0
	v_cvt_f32_u32_e32 v5, v4
	v_sub_u32_e32 v7, 0, v4
	v_rcp_iflag_f32_e32 v5, v5
	s_nop 0
	v_mul_f32_e32 v5, 0x4f7ffffe, v5
	v_cvt_u32_f32_e32 v5, v5
	v_mul_lo_u32 v7, v7, v5
	v_mul_hi_u32 v7, v5, v7
	v_add_u32_e32 v5, v5, v7
	s_waitcnt vmcnt(0) lgkmcnt(0)
	buffer_inv sc1
	v_mul_hi_u32 v5, v6, v5
	v_mul_lo_u32 v7, v5, v4
	v_sub_u32_e32 v7, v6, v7
	v_cmp_ge_u32_e32 vcc, v7, v4
	v_add_u32_e32 v8, 1, v5
	s_nop 0
	v_cndmask_b32_e32 v5, v5, v8, vcc
	v_sub_u32_e32 v8, v7, v4
	v_cndmask_b32_e32 v7, v7, v8, vcc
	v_cmp_ge_u32_e32 vcc, v7, v4
	v_add_u32_e32 v7, 1, v5
	v_add_u32_e32 v8, 1, v6
	v_cndmask_b32_e32 v5, v5, v7, vcc
	v_mad_u64_u32 v[6:7], s[10:11], v4, v5, v[4:5]
	v_cmp_ne_u32_e32 vcc, v8, v6
	s_and_saveexec_b64 s[10:11], vcc
	s_xor_b64 s[10:11], exec, s[10:11]
	s_cbranch_execz .LBB0_590
	s_add_i32 s48, s30, 0x900
	s_lshl_b64 s[12:13], s[48:49], 2
	s_add_u32 s14, s6, s12
	s_addc_u32 s15, s7, s13
	v_mov_b64_e32 v[6:7], s[14:15]
	flat_load_dword v2, v[6:7] sc1
	s_waitcnt vmcnt(0) lgkmcnt(0)
	v_cmp_eq_u32_e32 vcc, v2, v5
	s_and_saveexec_b64 s[12:13], vcc
	s_cbranch_execz .LBB0_589
	s_mov_b32 s31, 1
	s_mov_b64 s[16:17], 0
	s_branch .LBB0_581

.LBB0_589:
	s_or_b64 exec, exec, s[12:13]
	s_waitcnt vmcnt(0) lgkmcnt(0)
	s_waitcnt vmcnt(0)

.LBB0_626:
	s_and_b64 vcc, exec, s[0:1]
	s_cbranch_vccz .LBB0_661
	v_mov_b32_e32 v74, v233
	s_add_i32 s0, s55, 0xfffffec0
	v_writelane_b32 v255, s91, 52
	v_readfirstlane_b32 s1, v74
	s_ashr_i32 s10, s1, 6
	s_lshl_b32 s1, s0, 2
	s_and_b32 s1, s1, 0x7fffffe0
	s_lshl_b32 s4, s10, 2
	s_lshl_b32 s0, s0, 11
	s_sub_i32 s4, s4, s1
	s_and_b32 s5, s0, 0x3800
	s_mov_b32 s91, s45
	s_mov_b32 s45, s44
	s_mov_b32 s44, s81
	s_add_i32 s81, s4, 0x7e0
	s_lshl_b32 s0, s5, 8
	v_bfe_u32 v191, v74, 4, 2
	s_add_u32 s0, s85, s0
	s_addc_u32 s1, s88, 0
	v_or_b32_e32 v75, s81, v191
	s_add_i32 s81, s81, s5
	v_bfe_u32 v2, v74, 2, 2
	v_or_b32_e32 v4, s81, v2
	v_ashrrev_i32_e32 v5, 31, v4
	v_lshlrev_b64 v[4:5], 9, v[4:5]
	v_lshlrev_b32_e32 v2, 6, v74
	v_lshl_add_u64 v[4:5], s[52:53], 0, v[4:5]
	v_and_b32_e32 v2, 0xc0, v2
	v_lshl_add_u64 v[4:5], v[4:5], 0, v[2:3]
	v_and_b32_e32 v2, 48, v74
	v_add_u32_e32 v6, s5, v75
	v_lshl_add_u64 v[4:5], v[4:5], 0, v[2:3]
	v_ashrrev_i32_e32 v7, 31, v6
	s_mov_b32 s5, 0xbc00000
	v_lshl_add_u64 v[6:7], v[6:7], 4, s[66:67]
	v_add_co_u32_e32 v4, vcc, s5, v4
	global_load_dwordx4 v[8:11], v[6:7], off
	s_nop 0
	v_addc_co_u32_e32 v5, vcc, 0, v5, vcc
	global_load_dwordx4 v[4:7], v[4:5], off offset:256
	v_and_b32_e32 v76, 15, v74
	s_addk_i32 s4, 0x7e3
	v_mov_b32_e32 v13, v3
	v_lshlrev_b32_e32 v12, 8, v76
	s_ashr_i32 s5, s4, 31
	v_lshl_add_u64 v[12:13], s[0:1], 0, v[12:13]
	s_lshr_b32 s0, s5, 28
	s_add_i32 s4, s4, s0
	s_ashr_i32 s0, s4, 4
	s_add_i32 s0, s0, 16
	s_ashr_i32 s11, s0, 4
	s_cmp_gt_i32 s11, 0
	s_cselect_b64 s[20:21], -1, 0
	s_cmp_lt_i32 s11, 1
	v_lshl_add_u64 v[72:73], v[12:13], 0, v[2:3]
	s_waitcnt vmcnt(1)
	v_mul_f32_e32 v200, 0x3db504f3, v8
	v_mul_f32_e32 v199, 0x3db504f3, v9
	v_mul_f32_e32 v198, 0x3db504f3, v10
	v_mul_f32_e32 v192, 0x3db504f3, v11
	s_sub_i32 s12, s0, 14
	s_and_b32 s12, s12, -2
	s_mov_b32 s13, s10
	s_lshl_b32 s14, s10, 12
	s_mov_b32 s15, 0
	s_lshl_b32 s16, s10, 10
	s_add_i32 s16, s16, s65
.Lstgl_loop:
	s_cmp_ge_u32 s13, s12
	s_cbranch_scc1 .Lstgl_done
	v_lshl_add_u64 v[8:9], v[72:73], 0, s[14:15]
	s_mov_b32 m0, s16
	s_add_u32 s13, s13, 8
	global_load_lds_dwordx4 v[8:9], off
	s_add_u32 s14, s14, 0x8000
	s_add_u32 s16, s16, 0x2000
	s_branch .Lstgl_loop
.Lstgl_done:
	s_cmp_gt_i32 s11, 1
	s_cselect_b64 s[0:1], -1, 0
	s_cmp_gt_i32 s11, 2
	s_cselect_b64 s[92:93], -1, 0
	s_cmp_gt_i32 s11, 3
	s_cselect_b64 s[6:7], -1, 0
	s_cmp_gt_i32 s11, 4
	s_cselect_b64 s[70:71], -1, 0
	s_cmp_gt_i32 s11, 5
	s_cselect_b64 s[72:73], -1, 0
	s_cmp_gt_i32 s11, 6
	s_cselect_b64 s[56:57], -1, 0
	s_cmp_gt_i32 s11, 7
	s_cselect_b64 s[62:63], -1, 0
	v_and_b32_e32 v74, 63, v74
	v_mov_b32_e32 v78, 0
	v_mov_b32_e32 v77, 0
	v_mov_b32_e32 v80, 0
	v_mov_b32_e32 v79, 0
	v_mov_b32_e32 v82, 0
	v_mov_b32_e32 v81, 0
	v_mov_b32_e32 v84, 0
	v_mov_b32_e32 v83, 0
	v_mov_b32_e32 v86, 0
	v_mov_b32_e32 v85, 0
	v_mov_b32_e32 v88, 0
	v_mov_b32_e32 v87, 0
	v_mov_b32_e32 v90, 0
	v_mov_b32_e32 v89, 0
	v_mov_b32_e32 v92, 0
	v_mov_b32_e32 v91, 0
	v_mov_b32_e32 v94, 0
	v_mov_b32_e32 v93, 0
	v_mov_b32_e32 v96, 0
	v_mov_b32_e32 v95, 0
	v_mov_b32_e32 v98, 0
	v_mov_b32_e32 v97, 0
	v_mov_b32_e32 v100, 0
	v_mov_b32_e32 v99, 0
	v_mov_b32_e32 v102, 0
	v_mov_b32_e32 v101, 0
	v_mov_b32_e32 v104, 0
	v_mov_b32_e32 v103, 0
	v_mov_b32_e32 v106, 0
	v_mov_b32_e32 v105, 0
	v_mov_b32_e32 v108, 0
	v_mov_b32_e32 v107, 0
	v_mov_b32_e32 v110, 0
	v_mov_b32_e32 v109, 0
	v_mov_b32_e32 v112, 0
	v_mov_b32_e32 v111, 0
	v_mov_b32_e32 v114, 0
	v_mov_b32_e32 v113, 0
	v_mov_b32_e32 v116, 0
	v_mov_b32_e32 v115, 0
	v_mov_b32_e32 v118, 0
	v_mov_b32_e32 v117, 0
	v_mov_b32_e32 v120, 0
	v_mov_b32_e32 v119, 0
	v_mov_b32_e32 v122, 0
	v_mov_b32_e32 v121, 0
	v_mov_b32_e32 v124, 0
	v_mov_b32_e32 v123, 0
	v_mov_b32_e32 v126, 0
	v_mov_b32_e32 v125, 0
	v_mov_b32_e32 v128, 0
	v_mov_b32_e32 v127, 0
	v_mov_b32_e32 v130, 0
	v_mov_b32_e32 v129, 0
	v_mov_b32_e32 v132, 0
	v_mov_b32_e32 v131, 0
	v_mov_b32_e32 v134, 0
	v_mov_b32_e32 v133, 0
	v_mov_b32_e32 v136, 0
	v_mov_b32_e32 v135, 0
	v_mov_b32_e32 v138, 0
	v_mov_b32_e32 v137, 0
	v_mov_b32_e32 v140, 0
	v_mov_b32_e32 v139, 0
	v_mov_b32_e32 v142, 0
	v_mov_b32_e32 v141, 0
	v_mov_b32_e32 v144, 0
	v_mov_b32_e32 v143, 0
	v_mov_b32_e32 v146, 0
	v_mov_b32_e32 v145, 0
	v_mov_b32_e32 v148, 0
	v_mov_b32_e32 v147, 0
	v_mov_b32_e32 v150, 0
	v_mov_b32_e32 v149, 0
	v_mov_b32_e32 v152, 0
	v_mov_b32_e32 v151, 0
	v_mov_b32_e32 v154, 0
	v_mov_b32_e32 v153, 0
	v_mov_b32_e32 v156, 0
	v_mov_b32_e32 v155, 0
	v_mov_b32_e32 v158, 0
	v_mov_b32_e32 v157, 0
	v_mov_b32_e32 v160, 0
	v_mov_b32_e32 v159, 0
	v_mov_b32_e32 v162, 0
	v_mov_b32_e32 v161, 0
	v_mov_b32_e32 v164, 0
	v_mov_b32_e32 v163, 0
	v_mov_b32_e32 v166, 0
	v_mov_b32_e32 v165, 0
	v_mov_b32_e32 v168, 0
	v_mov_b32_e32 v167, 0
	v_mov_b32_e32 v170, 0
	v_mov_b32_e32 v169, 0
	v_mov_b32_e32 v172, 0
	v_mov_b32_e32 v171, 0
	v_mov_b32_e32 v174, 0
	v_mov_b32_e32 v173, 0
	v_mov_b32_e32 v176, 0
	v_mov_b32_e32 v175, 0
	v_mov_b32_e32 v178, 0
	v_mov_b32_e32 v177, 0
	v_mov_b32_e32 v180, 0
	v_mov_b32_e32 v179, 0
	v_mov_b32_e32 v182, 0
	v_mov_b32_e32 v181, 0
	v_mov_b32_e32 v184, 0
	v_mov_b32_e32 v183, 0
	v_mov_b32_e32 v186, 0
	v_mov_b32_e32 v185, 0
	v_mov_b32_e32 v188, 0
	v_mov_b32_e32 v187, 0
	v_lshl_add_u32 v0, v74, 4, s65
	s_mov_b32 s13, 0
	s_mov_b32 s14, 0
	s_waitcnt vmcnt(0)
	s_barrier
.Lscl_loop:
	s_cmp_ge_i32 s13, s11
	s_cbranch_scc1 .Lscl_done
	ds_read_b128 v[8:11], v0 offset:0
	ds_read_b128 v[12:15], v0 offset:1024
	ds_read_b128 v[16:19], v0 offset:2048
	ds_read_b128 v[20:23], v0 offset:3072
	ds_read_b128 v[24:27], v0 offset:4096
	ds_read_b128 v[28:31], v0 offset:5120
	ds_read_b128 v[32:35], v0 offset:6144
	ds_read_b128 v[36:39], v0 offset:7168
	ds_read_b128 v[40:43], v0 offset:8192
	ds_read_b128 v[44:47], v0 offset:9216
	ds_read_b128 v[48:51], v0 offset:10240
	ds_read_b128 v[52:55], v0 offset:11264
	ds_read_b128 v[56:59], v0 offset:12288
	ds_read_b128 v[60:63], v0 offset:13312
	ds_read_b128 v[64:67], v0 offset:14336
	ds_read_b128 v[68:71], v0 offset:15360
	s_waitcnt lgkmcnt(0)
	v_mfma_f32_16x16x32_bf16 v[8:11], v[4:7], v[8:11], 0
	v_mfma_f32_16x16x32_bf16 v[12:15], v[4:7], v[12:15], 0
	v_mfma_f32_16x16x32_bf16 v[16:19], v[4:7], v[16:19], 0
	v_mfma_f32_16x16x32_bf16 v[20:23], v[4:7], v[20:23], 0
	v_mfma_f32_16x16x32_bf16 v[24:27], v[4:7], v[24:27], 0
	v_mfma_f32_16x16x32_bf16 v[28:31], v[4:7], v[28:31], 0
	v_mfma_f32_16x16x32_bf16 v[32:35], v[4:7], v[32:35], 0
	v_mfma_f32_16x16x32_bf16 v[36:39], v[4:7], v[36:39], 0
	v_mfma_f32_16x16x32_bf16 v[40:43], v[4:7], v[40:43], 0
	v_mfma_f32_16x16x32_bf16 v[44:47], v[4:7], v[44:47], 0
	v_mfma_f32_16x16x32_bf16 v[48:51], v[4:7], v[48:51], 0
	v_mfma_f32_16x16x32_bf16 v[52:55], v[4:7], v[52:55], 0
	v_mfma_f32_16x16x32_bf16 v[56:59], v[4:7], v[56:59], 0
	v_mfma_f32_16x16x32_bf16 v[60:63], v[4:7], v[60:63], 0
	v_mfma_f32_16x16x32_bf16 v[64:67], v[4:7], v[64:67], 0
	v_mfma_f32_16x16x32_bf16 v[68:71], v[4:7], v[68:71], 0
	v_max_f32_e32 v8, 0, v8
	v_max_f32_e32 v9, 0, v9
	v_max_f32_e32 v10, 0, v10
	v_max_f32_e32 v11, 0, v11
	v_mul_f32_e32 v8, v200, v8
	v_fmac_f32_e32 v8, v9, v199
	v_fmac_f32_e32 v8, v10, v198
	v_fmac_f32_e32 v8, v11, v192
	v_sub_u32_e32 v11, v75, v76
	v_ashrrev_i32_e32 v11, 4, v11
	v_cmp_le_i32_e32 vcc, s14, v11
	v_ashrrev_i32_e32 v9, 31, v8
	v_or_b32_e32 v9, 0x80000000, v9
	v_xor_b32_e32 v8, v8, v9
	v_cndmask_b32_e32 v8, 0, v8, vcc
	v_max_f32_e32 v12, 0, v12
	v_max_f32_e32 v13, 0, v13
	v_max_f32_e32 v14, 0, v14
	v_max_f32_e32 v15, 0, v15
	v_mul_f32_e32 v12, v200, v12
	v_fmac_f32_e32 v12, v13, v199
	v_fmac_f32_e32 v12, v14, v198
	v_fmac_f32_e32 v12, v15, v192
	s_add_i32 s15, s14, 1
	v_cmp_le_i32_e32 vcc, s15, v11
	v_ashrrev_i32_e32 v13, 31, v12
	v_or_b32_e32 v13, 0x80000000, v13
	v_xor_b32_e32 v12, v12, v13
	v_cndmask_b32_e32 v12, 0, v12, vcc
	v_max_f32_e32 v16, 0, v16
	v_max_f32_e32 v17, 0, v17
	v_max_f32_e32 v18, 0, v18
	v_max_f32_e32 v19, 0, v19
	v_mul_f32_e32 v16, v200, v16
	v_fmac_f32_e32 v16, v17, v199
	v_fmac_f32_e32 v16, v18, v198
	v_fmac_f32_e32 v16, v19, v192
	s_add_i32 s15, s14, 2
	v_cmp_le_i32_e32 vcc, s15, v11
	v_ashrrev_i32_e32 v17, 31, v16
	v_or_b32_e32 v17, 0x80000000, v17
	v_xor_b32_e32 v16, v16, v17
	v_cndmask_b32_e32 v16, 0, v16, vcc
	v_max_f32_e32 v20, 0, v20
	v_max_f32_e32 v21, 0, v21
	v_max_f32_e32 v22, 0, v22
	v_max_f32_e32 v23, 0, v23
	v_mul_f32_e32 v20, v200, v20
	v_fmac_f32_e32 v20, v21, v199
	v_fmac_f32_e32 v20, v22, v198
	v_fmac_f32_e32 v20, v23, v192
	s_add_i32 s15, s14, 3
	v_cmp_le_i32_e32 vcc, s15, v11
	v_ashrrev_i32_e32 v21, 31, v20
	v_or_b32_e32 v21, 0x80000000, v21
	v_xor_b32_e32 v20, v20, v21
	v_cndmask_b32_e32 v20, 0, v20, vcc
	v_max_f32_e32 v24, 0, v24
	v_max_f32_e32 v25, 0, v25
	v_max_f32_e32 v26, 0, v26
	v_max_f32_e32 v27, 0, v27
	v_mul_f32_e32 v24, v200, v24
	v_fmac_f32_e32 v24, v25, v199
	v_fmac_f32_e32 v24, v26, v198
	v_fmac_f32_e32 v24, v27, v192
	s_add_i32 s15, s14, 4
	v_cmp_le_i32_e32 vcc, s15, v11
	v_ashrrev_i32_e32 v25, 31, v24
	v_or_b32_e32 v25, 0x80000000, v25
	v_xor_b32_e32 v24, v24, v25
	v_cndmask_b32_e32 v24, 0, v24, vcc
	v_max_f32_e32 v28, 0, v28
	v_max_f32_e32 v29, 0, v29
	v_max_f32_e32 v30, 0, v30
	v_max_f32_e32 v31, 0, v31
	v_mul_f32_e32 v28, v200, v28
	v_fmac_f32_e32 v28, v29, v199
	v_fmac_f32_e32 v28, v30, v198
	v_fmac_f32_e32 v28, v31, v192
	s_add_i32 s15, s14, 5
	v_cmp_le_i32_e32 vcc, s15, v11
	v_ashrrev_i32_e32 v29, 31, v28
	v_or_b32_e32 v29, 0x80000000, v29
	v_xor_b32_e32 v28, v28, v29
	v_cndmask_b32_e32 v28, 0, v28, vcc
	v_max_f32_e32 v32, 0, v32
	v_max_f32_e32 v33, 0, v33
	v_max_f32_e32 v34, 0, v34
	v_max_f32_e32 v35, 0, v35
	v_mul_f32_e32 v32, v200, v32
	v_fmac_f32_e32 v32, v33, v199
	v_fmac_f32_e32 v32, v34, v198
	v_fmac_f32_e32 v32, v35, v192
	s_add_i32 s15, s14, 6
	v_cmp_le_i32_e32 vcc, s15, v11
	v_ashrrev_i32_e32 v33, 31, v32
	v_or_b32_e32 v33, 0x80000000, v33
	v_xor_b32_e32 v32, v32, v33
	v_cndmask_b32_e32 v32, 0, v32, vcc
	v_max_f32_e32 v36, 0, v36
	v_max_f32_e32 v37, 0, v37
	v_max_f32_e32 v38, 0, v38
	v_max_f32_e32 v39, 0, v39
	v_mul_f32_e32 v36, v200, v36
	v_fmac_f32_e32 v36, v37, v199
	v_fmac_f32_e32 v36, v38, v198
	v_fmac_f32_e32 v36, v39, v192
	s_add_i32 s15, s14, 7
	v_cmp_le_i32_e32 vcc, s15, v11
	v_ashrrev_i32_e32 v37, 31, v36
	v_or_b32_e32 v37, 0x80000000, v37
	v_xor_b32_e32 v36, v36, v37
	v_cndmask_b32_e32 v36, 0, v36, vcc
	v_max_f32_e32 v40, 0, v40
	v_max_f32_e32 v41, 0, v41
	v_max_f32_e32 v42, 0, v42
	v_max_f32_e32 v43, 0, v43
	v_mul_f32_e32 v40, v200, v40
	v_fmac_f32_e32 v40, v41, v199
	v_fmac_f32_e32 v40, v42, v198
	v_fmac_f32_e32 v40, v43, v192
	s_add_i32 s15, s14, 8
	v_cmp_le_i32_e32 vcc, s15, v11
	v_ashrrev_i32_e32 v41, 31, v40
	v_or_b32_e32 v41, 0x80000000, v41
	v_xor_b32_e32 v40, v40, v41
	v_cndmask_b32_e32 v40, 0, v40, vcc
	v_max_f32_e32 v44, 0, v44
	v_max_f32_e32 v45, 0, v45
	v_max_f32_e32 v46, 0, v46
	v_max_f32_e32 v47, 0, v47
	v_mul_f32_e32 v44, v200, v44
	v_fmac_f32_e32 v44, v45, v199
	v_fmac_f32_e32 v44, v46, v198
	v_fmac_f32_e32 v44, v47, v192
	s_add_i32 s15, s14, 9
	v_cmp_le_i32_e32 vcc, s15, v11
	v_ashrrev_i32_e32 v45, 31, v44
	v_or_b32_e32 v45, 0x80000000, v45
	v_xor_b32_e32 v44, v44, v45
	v_cndmask_b32_e32 v44, 0, v44, vcc
	v_max_f32_e32 v48, 0, v48
	v_max_f32_e32 v49, 0, v49
	v_max_f32_e32 v50, 0, v50
	v_max_f32_e32 v51, 0, v51
	v_mul_f32_e32 v48, v200, v48
	v_fmac_f32_e32 v48, v49, v199
	v_fmac_f32_e32 v48, v50, v198
	v_fmac_f32_e32 v48, v51, v192
	s_add_i32 s15, s14, 10
	v_cmp_le_i32_e32 vcc, s15, v11
	v_ashrrev_i32_e32 v49, 31, v48
	v_or_b32_e32 v49, 0x80000000, v49
	v_xor_b32_e32 v48, v48, v49
	v_cndmask_b32_e32 v48, 0, v48, vcc
	v_max_f32_e32 v52, 0, v52
	v_max_f32_e32 v53, 0, v53
	v_max_f32_e32 v54, 0, v54
	v_max_f32_e32 v55, 0, v55
	v_mul_f32_e32 v52, v200, v52
	v_fmac_f32_e32 v52, v53, v199
	v_fmac_f32_e32 v52, v54, v198
	v_fmac_f32_e32 v52, v55, v192
	s_add_i32 s15, s14, 11
	v_cmp_le_i32_e32 vcc, s15, v11
	v_ashrrev_i32_e32 v53, 31, v52
	v_or_b32_e32 v53, 0x80000000, v53
	v_xor_b32_e32 v52, v52, v53
	v_cndmask_b32_e32 v52, 0, v52, vcc
	v_max_f32_e32 v56, 0, v56
	v_max_f32_e32 v57, 0, v57
	v_max_f32_e32 v58, 0, v58
	v_max_f32_e32 v59, 0, v59
	v_mul_f32_e32 v56, v200, v56
	v_fmac_f32_e32 v56, v57, v199
	v_fmac_f32_e32 v56, v58, v198
	v_fmac_f32_e32 v56, v59, v192
	s_add_i32 s15, s14, 12
	v_cmp_le_i32_e32 vcc, s15, v11
	v_ashrrev_i32_e32 v57, 31, v56
	v_or_b32_e32 v57, 0x80000000, v57
	v_xor_b32_e32 v56, v56, v57
	v_cndmask_b32_e32 v56, 0, v56, vcc
	v_max_f32_e32 v60, 0, v60
	v_max_f32_e32 v61, 0, v61
	v_max_f32_e32 v62, 0, v62
	v_max_f32_e32 v63, 0, v63
	v_mul_f32_e32 v60, v200, v60
	v_fmac_f32_e32 v60, v61, v199
	v_fmac_f32_e32 v60, v62, v198
	v_fmac_f32_e32 v60, v63, v192
	s_add_i32 s15, s14, 13
	v_cmp_le_i32_e32 vcc, s15, v11
	v_ashrrev_i32_e32 v61, 31, v60
	v_or_b32_e32 v61, 0x80000000, v61
	v_xor_b32_e32 v60, v60, v61
	v_cndmask_b32_e32 v60, 0, v60, vcc
	v_max_f32_e32 v64, 0, v64
	v_max_f32_e32 v65, 0, v65
	v_max_f32_e32 v66, 0, v66
	v_max_f32_e32 v67, 0, v67
	v_mul_f32_e32 v64, v200, v64
	v_fmac_f32_e32 v64, v65, v199
	v_fmac_f32_e32 v64, v66, v198
	v_fmac_f32_e32 v64, v67, v192
	s_add_i32 s15, s14, 14
	v_cmp_le_i32_e32 vcc, s15, v11
	v_ashrrev_i32_e32 v65, 31, v64
	v_or_b32_e32 v65, 0x80000000, v65
	v_xor_b32_e32 v64, v64, v65
	v_cndmask_b32_e32 v64, 0, v64, vcc
	v_max_f32_e32 v68, 0, v68
	v_max_f32_e32 v69, 0, v69
	v_max_f32_e32 v70, 0, v70
	v_max_f32_e32 v71, 0, v71
	v_mul_f32_e32 v68, v200, v68
	v_fmac_f32_e32 v68, v69, v199
	v_fmac_f32_e32 v68, v70, v198
	v_fmac_f32_e32 v68, v71, v192
	s_add_i32 s15, s14, 15
	v_cmp_le_i32_e32 vcc, s15, v11
	v_ashrrev_i32_e32 v69, 31, v68
	v_or_b32_e32 v69, 0x80000000, v69
	v_xor_b32_e32 v68, v68, v69
	v_cndmask_b32_e32 v68, 0, v68, vcc
	s_cmp_lg_u32 s13, 0
	s_cbranch_scc1 .Lscl_co1
	v_mov_b32_e32 v78, v8
	v_mov_b32_e32 v77, v12
	v_mov_b32_e32 v80, v16
	v_mov_b32_e32 v79, v20
	v_mov_b32_e32 v82, v24
	v_mov_b32_e32 v81, v28
	v_mov_b32_e32 v84, v32
	v_mov_b32_e32 v83, v36
	v_mov_b32_e32 v86, v40
	v_mov_b32_e32 v85, v44
	v_mov_b32_e32 v88, v48
	v_mov_b32_e32 v87, v52
	v_mov_b32_e32 v90, v56
	v_mov_b32_e32 v89, v60
	v_mov_b32_e32 v92, v64
	v_mov_b32_e32 v91, v68
	s_branch .Lscl_next
.Lscl_co1:
	s_cmp_lg_u32 s13, 1
	s_cbranch_scc1 .Lscl_co2
	v_mov_b32_e32 v94, v8
	v_mov_b32_e32 v93, v12
	v_mov_b32_e32 v96, v16
	v_mov_b32_e32 v95, v20
	v_mov_b32_e32 v98, v24
	v_mov_b32_e32 v97, v28
	v_mov_b32_e32 v100, v32
	v_mov_b32_e32 v99, v36
	v_mov_b32_e32 v102, v40
	v_mov_b32_e32 v101, v44
	v_mov_b32_e32 v104, v48
	v_mov_b32_e32 v103, v52
	v_mov_b32_e32 v106, v56
	v_mov_b32_e32 v105, v60
	v_mov_b32_e32 v108, v64
	v_mov_b32_e32 v107, v68
	s_branch .Lscl_next
.Lscl_co2:
	s_cmp_lg_u32 s13, 2
	s_cbranch_scc1 .Lscl_co3
	v_mov_b32_e32 v110, v8
	v_mov_b32_e32 v109, v12
	v_mov_b32_e32 v112, v16
	v_mov_b32_e32 v111, v20
	v_mov_b32_e32 v114, v24
	v_mov_b32_e32 v113, v28
	v_mov_b32_e32 v116, v32
	v_mov_b32_e32 v115, v36
	v_mov_b32_e32 v118, v40
	v_mov_b32_e32 v117, v44
	v_mov_b32_e32 v120, v48
	v_mov_b32_e32 v119, v52
	v_mov_b32_e32 v122, v56
	v_mov_b32_e32 v121, v60
	v_mov_b32_e32 v124, v64
	v_mov_b32_e32 v123, v68
	s_branch .Lscl_next
.Lscl_co3:
	s_cmp_lg_u32 s13, 3
	s_cbranch_scc1 .Lscl_co4
	v_mov_b32_e32 v126, v8
	v_mov_b32_e32 v125, v12
	v_mov_b32_e32 v128, v16
	v_mov_b32_e32 v127, v20
	v_mov_b32_e32 v130, v24
	v_mov_b32_e32 v129, v28
	v_mov_b32_e32 v132, v32
	v_mov_b32_e32 v131, v36
	v_mov_b32_e32 v134, v40
	v_mov_b32_e32 v133, v44
	v_mov_b32_e32 v136, v48
	v_mov_b32_e32 v135, v52
	v_mov_b32_e32 v138, v56
	v_mov_b32_e32 v137, v60
	v_mov_b32_e32 v140, v64
	v_mov_b32_e32 v139, v68
	s_branch .Lscl_next
.Lscl_co4:
	s_cmp_lg_u32 s13, 4
	s_cbranch_scc1 .Lscl_co5
	v_mov_b32_e32 v142, v8
	v_mov_b32_e32 v141, v12
	v_mov_b32_e32 v144, v16
	v_mov_b32_e32 v143, v20
	v_mov_b32_e32 v146, v24
	v_mov_b32_e32 v145, v28
	v_mov_b32_e32 v148, v32
	v_mov_b32_e32 v147, v36
	v_mov_b32_e32 v150, v40
	v_mov_b32_e32 v149, v44
	v_mov_b32_e32 v152, v48
	v_mov_b32_e32 v151, v52
	v_mov_b32_e32 v154, v56
	v_mov_b32_e32 v153, v60
	v_mov_b32_e32 v156, v64
	v_mov_b32_e32 v155, v68
	s_branch .Lscl_next
.Lscl_co5:
	s_cmp_lg_u32 s13, 5
	s_cbranch_scc1 .Lscl_co6
	v_mov_b32_e32 v158, v8
	v_mov_b32_e32 v157, v12
	v_mov_b32_e32 v160, v16
	v_mov_b32_e32 v159, v20
	v_mov_b32_e32 v162, v24
	v_mov_b32_e32 v161, v28
	v_mov_b32_e32 v164, v32
	v_mov_b32_e32 v163, v36
	v_mov_b32_e32 v166, v40
	v_mov_b32_e32 v165, v44
	v_mov_b32_e32 v168, v48
	v_mov_b32_e32 v167, v52
	v_mov_b32_e32 v170, v56
	v_mov_b32_e32 v169, v60
	v_mov_b32_e32 v172, v64
	v_mov_b32_e32 v171, v68
	s_branch .Lscl_next
.Lscl_co6:
	s_cmp_lg_u32 s13, 6
	s_cbranch_scc1 .Lscl_co7
	v_mov_b32_e32 v174, v8
	v_mov_b32_e32 v173, v12
	v_mov_b32_e32 v176, v16
	v_mov_b32_e32 v175, v20
	v_mov_b32_e32 v178, v24
	v_mov_b32_e32 v177, v28
	v_mov_b32_e32 v180, v32
	v_mov_b32_e32 v179, v36
	v_mov_b32_e32 v182, v40
	v_mov_b32_e32 v181, v44
	v_mov_b32_e32 v184, v48
	v_mov_b32_e32 v183, v52
	v_mov_b32_e32 v186, v56
	v_mov_b32_e32 v185, v60
	v_mov_b32_e32 v188, v64
	v_mov_b32_e32 v187, v68
	s_branch .Lscl_next
.Lscl_co7:
	v_mov_b32_e32 v21, v64
	v_mov_b32_e32 v25, v56
	v_mov_b32_e32 v33, v48
	v_mov_b32_e32 v41, v40
	v_mov_b32_e32 v49, v32
	v_mov_b32_e32 v57, v24
	v_mov_b32_e32 v64, v20
	v_mov_b32_e32 v190, v8
	v_mov_b32_e32 v189, v12
	v_mov_b32_e32 v65, v16
	v_mov_b32_e32 v56, v28
	v_mov_b32_e32 v48, v36
	v_mov_b32_e32 v40, v44
	v_mov_b32_e32 v32, v52
	v_mov_b32_e32 v24, v60
	v_mov_b32_e32 v20, v68
.Lscl_next:
	s_add_i32 s13, s13, 1
	s_add_i32 s14, s14, 16
	v_add_u32_e32 v0, 0x4000, v0
	s_branch .Lscl_loop
.Lscl_done:
	s_cmp_gt_i32 s11, 7
	s_cbranch_scc1 .Lscl_fin
	v_mov_b32_e32 v190, 0
	v_mov_b32_e32 v189, 0
	v_mov_b32_e32 v65, 0
	v_mov_b32_e32 v64, 0
	v_mov_b32_e32 v57, 0
	v_mov_b32_e32 v56, 0
	v_mov_b32_e32 v49, 0
	v_mov_b32_e32 v48, 0
	v_mov_b32_e32 v41, 0
	v_mov_b32_e32 v40, 0
	v_mov_b32_e32 v33, 0
	v_mov_b32_e32 v32, 0
	v_mov_b32_e32 v25, 0
	v_mov_b32_e32 v24, 0
	v_mov_b32_e32 v21, 0
	v_mov_b32_e32 v20, 0
.Lscl_fin:
	s_barrier
	s_branch .LBB0_1320
.LBB0_661:
	s_mov_b64 s[0:1], 0

.LBB0_689:
	s_andn2_b64 vcc, exec, s[0:1]
	s_cbranch_vccnz .LBB0_612
	v_mov_b32_e32 v74, v233
	v_mov_b32_e32 v13, v3
	v_readfirstlane_b32 s0, v74
	s_ashr_i32 s10, s0, 6
	s_lshl_b32 s0, s55, 2
	s_andn2_b32 s0, s0, 31
	s_lshl_b32 s1, s10, 2
	s_sub_i32 s4, s1, s0
	s_lshl_b32 s0, s55, 11
	s_and_b32 s6, s0, 0x3800
	s_add_i32 s5, s4, 0x7e0
	s_lshl_b32 s0, s6, 8
	s_add_u32 s0, s85, s0
	s_addc_u32 s1, s88, 0
	s_add_i32 s55, s5, s6
	v_bfe_u32 v2, v74, 2, 2
	v_or_b32_e32 v4, s55, v2
	v_ashrrev_i32_e32 v5, 31, v4
	v_bfe_u32 v191, v74, 4, 2
	v_lshlrev_b64 v[4:5], 9, v[4:5]
	v_lshlrev_b32_e32 v2, 6, v74
	v_or_b32_e32 v75, s5, v191
	v_lshl_add_u64 v[4:5], s[52:53], 0, v[4:5]
	v_and_b32_e32 v2, 0xc0, v2
	v_lshl_add_u64 v[4:5], v[4:5], 0, v[2:3]
	v_and_b32_e32 v2, 48, v74
	v_add_u32_e32 v6, s6, v75
	v_lshl_add_u64 v[4:5], v[4:5], 0, v[2:3]
	v_ashrrev_i32_e32 v7, 31, v6
	s_mov_b32 s5, 0xbc00000
	v_lshl_add_u64 v[6:7], v[6:7], 4, s[66:67]
	v_add_co_u32_e32 v4, vcc, s5, v4
	global_load_dwordx4 v[8:11], v[6:7], off
	s_nop 0
	v_addc_co_u32_e32 v5, vcc, 0, v5, vcc
	global_load_dwordx4 v[4:7], v[4:5], off offset:256
	v_and_b32_e32 v76, 15, v74
	s_addk_i32 s4, 0x7e3
	v_lshlrev_b32_e32 v12, 8, v76
	s_ashr_i32 s5, s4, 31
	v_lshl_add_u64 v[12:13], s[0:1], 0, v[12:13]
	s_lshr_b32 s0, s5, 28
	s_add_i32 s4, s4, s0
	s_ashr_i32 s0, s4, 4
	s_add_i32 s0, s0, 16
	s_ashr_i32 s11, s0, 4
	s_cmp_gt_i32 s11, 0
	s_cselect_b64 s[20:21], -1, 0
	s_cmp_lt_i32 s11, 1
	v_lshl_add_u64 v[72:73], v[12:13], 0, v[2:3]
	s_waitcnt vmcnt(1)
	v_mul_f32_e32 v200, 0x3db504f3, v8
	v_mul_f32_e32 v199, 0x3db504f3, v9
	v_mul_f32_e32 v198, 0x3db504f3, v10
	v_mul_f32_e32 v192, 0x3db504f3, v11
	s_sub_i32 s12, s0, 14
	s_and_b32 s12, s12, -2
	s_mov_b32 s13, s10
	s_lshl_b32 s14, s10, 12
	s_mov_b32 s15, 0
	s_lshl_b32 s16, s10, 10
	s_add_i32 s16, s16, s65

.Lsch_fin:
	s_barrier
	s_branch .LBB0_963
.LBB0_963:
	s_mulk_i32 s10, 0x1200
	s_add_i32 s4, s65, s10
	s_waitcnt vmcnt(0)
	v_mov_b32_e32 v4, s4
	s_movk_i32 s4, 0x440
	v_mad_u32_u24 v27, v191, s4, v4
	v_lshl_add_u32 v28, v76, 6, v27
	v_mul_i32_i24_e32 v4, 0xffffffc4, v76
	v_lshlrev_b32_e32 v29, 4, v76
	v_lshlrev_b32_e32 v5, 2, v74
	v_mov_b32_e32 v23, 0x100
	v_or_b32_e32 v26, 0x100, v76
	v_add_u32_e32 v30, 4, v5
	v_cmp_eq_u32_e64 s[10:11], 15, v76
	v_add_u32_e32 v31, 8, v5
	v_cmp_gt_u32_e64 s[12:13], 14, v76
	v_add_u32_e32 v34, 16, v5
	v_cmp_gt_u32_e64 s[14:15], 12, v76
	v_add_u32_e32 v35, 32, v5
	v_cmp_gt_u32_e64 s[16:17], 8, v76
	v_or_b32_e32 v36, 15, v29
	v_or_b32_e32 v37, 14, v29
	v_or_b32_e32 v38, 13, v29
	v_or_b32_e32 v39, 12, v29
	v_or_b32_e32 v42, 11, v29
	v_or_b32_e32 v43, 10, v29
	v_or_b32_e32 v44, 9, v29
	v_or_b32_e32 v45, 8, v29
	v_or_b32_e32 v46, 7, v29
	v_or_b32_e32 v47, 6, v29
	v_or_b32_e32 v50, 5, v29
	v_or_b32_e32 v51, 4, v29
	v_or_b32_e32 v52, 3, v29
	v_or_b32_e32 v53, 2, v29
	v_or_b32_e32 v54, 1, v29
	v_mov_b32_e32 v22, 0
	s_mov_b32 s33, 24
	v_add_u32_e32 v55, v28, v4
	v_mov_b32_e32 v4, 0
	s_branch .LBB0_968

.LBB0_1080:
	v_cmp_ge_u32_e32 vcc, v190, v22
	v_cmp_eq_u32_e64 s[10:11], 48, v74
	s_nop 0
	v_mov_b32_e32 v2, vcc_lo
	v_cndmask_b32_e64 v2, v6, v2, s[10:11]
	v_mov_b32_e32 v6, vcc_hi
	v_cmp_ge_u32_e32 vcc, v189, v22
	v_cndmask_b32_e64 v6, v7, v6, s[10:11]
	v_cmp_eq_u32_e64 s[10:11], 49, v74
	v_mov_b32_e32 v7, vcc_hi
	s_nop 0
	v_cndmask_b32_e64 v6, v6, v7, s[10:11]
	v_mov_b32_e32 v7, vcc_lo
	v_cmp_ge_u32_e32 vcc, v65, v22
	v_cndmask_b32_e64 v2, v2, v7, s[10:11]
	v_cmp_eq_u32_e64 s[10:11], 50, v74
	v_mov_b32_e32 v7, vcc_lo
	s_nop 0
	v_cndmask_b32_e64 v2, v2, v7, s[10:11]
	v_mov_b32_e32 v7, vcc_hi
	v_cmp_ge_u32_e32 vcc, v64, v22
	v_cndmask_b32_e64 v6, v6, v7, s[10:11]
	v_cmp_eq_u32_e64 s[10:11], 51, v74
	v_mov_b32_e32 v7, vcc_hi
	s_nop 0
	v_cndmask_b32_e64 v6, v6, v7, s[10:11]
	v_mov_b32_e32 v7, vcc_lo
	v_cmp_ge_u32_e32 vcc, v57, v22
	v_cndmask_b32_e64 v2, v2, v7, s[10:11]
	v_cmp_eq_u32_e64 s[10:11], 52, v74
	v_mov_b32_e32 v7, vcc_lo
	s_nop 0
	v_cndmask_b32_e64 v2, v2, v7, s[10:11]
	v_mov_b32_e32 v7, vcc_hi
	v_cmp_ge_u32_e32 vcc, v56, v22
	v_cndmask_b32_e64 v6, v6, v7, s[10:11]
	v_cmp_eq_u32_e64 s[10:11], 53, v74
	v_mov_b32_e32 v7, vcc_hi
	s_nop 0
	v_cndmask_b32_e64 v6, v6, v7, s[10:11]
	v_mov_b32_e32 v7, vcc_lo
	v_cmp_ge_u32_e32 vcc, v49, v22
	v_cndmask_b32_e64 v2, v2, v7, s[10:11]
	v_cmp_eq_u32_e64 s[10:11], 54, v74
	v_mov_b32_e32 v7, vcc_lo
	s_nop 0
	v_cndmask_b32_e64 v2, v2, v7, s[10:11]
	v_mov_b32_e32 v7, vcc_hi
	v_cmp_ge_u32_e32 vcc, v48, v22
	v_cndmask_b32_e64 v6, v6, v7, s[10:11]
	v_cmp_eq_u32_e64 s[10:11], 55, v74
	v_mov_b32_e32 v7, vcc_hi
	s_nop 0
	v_cndmask_b32_e64 v6, v6, v7, s[10:11]
	v_mov_b32_e32 v7, vcc_lo
	v_cmp_ge_u32_e32 vcc, v41, v22
	v_cndmask_b32_e64 v2, v2, v7, s[10:11]
	v_cmp_eq_u32_e64 s[10:11], 56, v74
	v_mov_b32_e32 v7, vcc_lo
	s_nop 0
	v_cndmask_b32_e64 v2, v2, v7, s[10:11]
	v_mov_b32_e32 v7, vcc_hi
	v_cmp_ge_u32_e32 vcc, v40, v22
	v_cndmask_b32_e64 v6, v6, v7, s[10:11]
	v_cmp_eq_u32_e64 s[10:11], 57, v74
	v_mov_b32_e32 v7, vcc_hi
	s_nop 0
	v_cndmask_b32_e64 v6, v6, v7, s[10:11]
	v_mov_b32_e32 v7, vcc_lo
	v_cmp_ge_u32_e32 vcc, v33, v22
	v_cndmask_b32_e64 v2, v2, v7, s[10:11]
	v_cmp_eq_u32_e64 s[10:11], 58, v74
	v_mov_b32_e32 v7, vcc_lo
	s_nop 0
	v_cndmask_b32_e64 v2, v2, v7, s[10:11]
	v_mov_b32_e32 v7, vcc_hi
	v_cmp_ge_u32_e32 vcc, v32, v22
	v_cndmask_b32_e64 v6, v6, v7, s[10:11]
	v_cmp_eq_u32_e64 s[10:11], 59, v74
	v_mov_b32_e32 v7, vcc_hi
	s_nop 0
	v_cndmask_b32_e64 v6, v6, v7, s[10:11]
	v_mov_b32_e32 v7, vcc_lo
	v_cmp_ge_u32_e32 vcc, v25, v22
	v_cndmask_b32_e64 v2, v2, v7, s[10:11]
	v_cmp_eq_u32_e64 s[10:11], 60, v74
	v_mov_b32_e32 v7, vcc_lo
	s_nop 0
	v_cndmask_b32_e64 v2, v2, v7, s[10:11]
	v_mov_b32_e32 v7, vcc_hi
	v_cmp_ge_u32_e32 vcc, v24, v22
	v_cndmask_b32_e64 v6, v6, v7, s[10:11]
	v_cmp_eq_u32_e64 s[10:11], 61, v74
	v_mov_b32_e32 v7, vcc_hi
	s_nop 0
	v_cndmask_b32_e64 v6, v6, v7, s[10:11]
	v_mov_b32_e32 v7, vcc_lo
	v_cmp_ge_u32_e32 vcc, v21, v22
	v_cndmask_b32_e64 v2, v2, v7, s[10:11]
	v_cmp_eq_u32_e64 s[10:11], 62, v74
	v_mov_b32_e32 v7, vcc_lo
	s_nop 0
	v_cndmask_b32_e64 v2, v2, v7, s[10:11]
	v_mov_b32_e32 v7, vcc_hi
	v_cmp_ge_u32_e32 vcc, v20, v22
	v_cndmask_b32_e64 v6, v6, v7, s[10:11]
	v_cmp_eq_u32_e64 s[10:11], 63, v74
	v_mov_b32_e32 v7, vcc_hi
	s_nop 0
	v_cndmask_b32_e64 v7, v6, v7, s[10:11]
	v_mov_b32_e32 v6, vcc_lo
	v_cndmask_b32_e64 v6, v2, v6, s[10:11]
	s_branch .LBB0_611
.LBB0_1320:
	s_mulk_i32 s10, 0x1200
	s_add_i32 s4, s65, s10
	s_waitcnt vmcnt(0)
	v_mov_b32_e32 v4, s4
	s_movk_i32 s4, 0x440
	v_mad_u32_u24 v27, v191, s4, v4
	v_lshl_add_u32 v28, v76, 6, v27
	v_mul_i32_i24_e32 v4, 0xffffffc4, v76
	v_lshlrev_b32_e32 v29, 4, v76
	v_lshlrev_b32_e32 v5, 2, v74
	v_mov_b32_e32 v23, 0x100
	v_or_b32_e32 v26, 0x100, v76
	v_add_u32_e32 v30, 4, v5
	v_cmp_eq_u32_e64 s[10:11], 15, v76
	v_add_u32_e32 v31, 8, v5
	v_cmp_gt_u32_e64 s[12:13], 14, v76
	v_add_u32_e32 v34, 16, v5
	v_cmp_gt_u32_e64 s[14:15], 12, v76
	v_add_u32_e32 v35, 32, v5
	v_cmp_gt_u32_e64 s[16:17], 8, v76
	v_or_b32_e32 v36, 15, v29
	v_or_b32_e32 v37, 14, v29
	v_or_b32_e32 v38, 13, v29
	v_or_b32_e32 v39, 12, v29
	v_or_b32_e32 v42, 11, v29
	v_or_b32_e32 v43, 10, v29
	v_or_b32_e32 v44, 9, v29
	v_or_b32_e32 v45, 8, v29
	v_or_b32_e32 v46, 7, v29
	v_or_b32_e32 v47, 6, v29
	v_or_b32_e32 v50, 5, v29
	v_or_b32_e32 v51, 4, v29
	v_or_b32_e32 v52, 3, v29
	v_or_b32_e32 v53, 2, v29
	v_or_b32_e32 v54, 1, v29
	v_mov_b32_e32 v22, 0
	s_mov_b32 s33, 24
	v_add_u32_e32 v55, v28, v4
	v_mov_b32_e32 v4, 0
	s_branch .LBB0_1325

.LBB0_1456:
	s_lshl_b32 s28, s42, 6
	s_add_i32 s48, s28, 0x500
	s_lshl_b64 s[6:7], s[48:49], 2
	s_add_u32 s6, s4, s6
	s_addc_u32 s7, s5, s7
	v_mov_b64_e32 v[6:7], s[6:7]
	flat_atomic_add v6, v[6:7], v232 sc0
	v_cvt_f32_u32_e32 v5, v4
	v_sub_u32_e32 v7, 0, v4
	v_rcp_iflag_f32_e32 v5, v5
	s_nop 0
	v_mul_f32_e32 v5, 0x4f7ffffe, v5
	v_cvt_u32_f32_e32 v5, v5
	v_mul_lo_u32 v7, v7, v5
	v_mul_hi_u32 v7, v5, v7
	v_add_u32_e32 v5, v5, v7
	s_waitcnt vmcnt(0) lgkmcnt(0)
	buffer_inv sc1
	v_mul_hi_u32 v5, v6, v5
	v_mul_lo_u32 v7, v5, v4
	v_sub_u32_e32 v7, v6, v7
	v_cmp_ge_u32_e32 vcc, v7, v4
	v_add_u32_e32 v8, 1, v5
	s_nop 0
	v_cndmask_b32_e32 v5, v5, v8, vcc
	v_sub_u32_e32 v8, v7, v4
	v_cndmask_b32_e32 v7, v7, v8, vcc
	v_cmp_ge_u32_e32 vcc, v7, v4
	v_add_u32_e32 v7, 1, v5
	v_add_u32_e32 v8, 1, v6
	v_cndmask_b32_e32 v5, v5, v7, vcc
	v_mad_u64_u32 v[6:7], s[6:7], v4, v5, v[4:5]
	v_cmp_ne_u32_e32 vcc, v8, v6
	s_and_saveexec_b64 s[6:7], vcc
	s_xor_b64 s[6:7], exec, s[6:7]
	s_cbranch_execz .LBB0_1469
	s_add_i32 s48, s28, 0x900
	s_lshl_b64 s[10:11], s[48:49], 2
	s_add_u32 s12, s4, s10
	s_addc_u32 s13, s5, s11
	v_mov_b64_e32 v[6:7], s[12:13]
	flat_load_dword v2, v[6:7] sc1
	s_waitcnt vmcnt(0) lgkmcnt(0)
	v_cmp_eq_u32_e32 vcc, v2, v5
	s_and_saveexec_b64 s[10:11], vcc
	s_cbranch_execz .LBB0_1468
	s_mov_b32 s29, 1
	s_mov_b64 s[14:15], 0
	s_branch .LBB0_1460

.LBB0_1468:
	s_or_b64 exec, exec, s[10:11]
	s_waitcnt vmcnt(0) lgkmcnt(0)
	s_waitcnt vmcnt(0)

.LBB0_1946:
	s_lshl_b32 s28, s33, 6
	s_add_i32 s48, s28, 0x500
	s_lshl_b64 s[6:7], s[48:49], 2
	s_add_u32 s6, s4, s6
	s_addc_u32 s7, s5, s7
	v_mov_b64_e32 v[6:7], s[6:7]
	flat_atomic_add v6, v[6:7], v232 sc0
	v_cvt_f32_u32_e32 v5, v4
	v_sub_u32_e32 v7, 0, v4
	v_rcp_iflag_f32_e32 v5, v5
	s_nop 0
	v_mul_f32_e32 v5, 0x4f7ffffe, v5
	v_cvt_u32_f32_e32 v5, v5
	v_mul_lo_u32 v7, v7, v5
	v_mul_hi_u32 v7, v5, v7
	v_add_u32_e32 v5, v5, v7
	s_waitcnt vmcnt(0) lgkmcnt(0)
	buffer_inv sc1
	v_mul_hi_u32 v5, v6, v5
	v_mul_lo_u32 v7, v5, v4
	v_sub_u32_e32 v7, v6, v7
	v_cmp_ge_u32_e32 vcc, v7, v4
	v_add_u32_e32 v8, 1, v5
	s_nop 0
	v_cndmask_b32_e32 v5, v5, v8, vcc
	v_sub_u32_e32 v8, v7, v4
	v_cndmask_b32_e32 v7, v7, v8, vcc
	v_cmp_ge_u32_e32 vcc, v7, v4
	v_add_u32_e32 v7, 1, v5
	v_add_u32_e32 v8, 1, v6
	v_cndmask_b32_e32 v5, v5, v7, vcc
	v_mad_u64_u32 v[6:7], s[6:7], v4, v5, v[4:5]
	v_cmp_ne_u32_e32 vcc, v8, v6
	s_and_saveexec_b64 s[6:7], vcc
	s_xor_b64 s[6:7], exec, s[6:7]
	s_cbranch_execz .LBB0_1959
	s_add_i32 s48, s28, 0x900
	s_lshl_b64 s[10:11], s[48:49], 2
	s_add_u32 s12, s4, s10
	s_addc_u32 s13, s5, s11
	v_mov_b64_e32 v[6:7], s[12:13]
	flat_load_dword v2, v[6:7] sc1
	s_waitcnt vmcnt(0) lgkmcnt(0)
	v_cmp_eq_u32_e32 vcc, v2, v5
	s_and_saveexec_b64 s[10:11], vcc
	s_cbranch_execz .LBB0_1958
	s_mov_b32 s29, 1
	s_mov_b64 s[14:15], 0
	s_branch .LBB0_1950

.LBB0_2125:
	s_lshl_b32 s30, s42, 6
	s_add_i32 s48, s30, 0x500
	s_lshl_b64 s[10:11], s[48:49], 2
	s_add_u32 s10, s4, s10
	s_addc_u32 s11, s5, s11
	v_mov_b64_e32 v[6:7], s[10:11]
	flat_atomic_add v6, v[6:7], v232 sc0
	v_cvt_f32_u32_e32 v5, v4
	v_sub_u32_e32 v7, 0, v4
	v_rcp_iflag_f32_e32 v5, v5
	s_nop 0
	v_mul_f32_e32 v5, 0x4f7ffffe, v5
	v_cvt_u32_f32_e32 v5, v5
	v_mul_lo_u32 v7, v7, v5
	v_mul_hi_u32 v7, v5, v7
	v_add_u32_e32 v5, v5, v7
	s_waitcnt vmcnt(0) lgkmcnt(0)
	buffer_inv sc1
	v_mul_hi_u32 v5, v6, v5
	v_mul_lo_u32 v7, v5, v4
	v_sub_u32_e32 v7, v6, v7
	v_cmp_ge_u32_e32 vcc, v7, v4
	v_add_u32_e32 v8, 1, v5
	s_nop 0
	v_cndmask_b32_e32 v5, v5, v8, vcc
	v_sub_u32_e32 v8, v7, v4
	v_cndmask_b32_e32 v7, v7, v8, vcc
	v_cmp_ge_u32_e32 vcc, v7, v4
	v_add_u32_e32 v7, 1, v5
	v_add_u32_e32 v8, 1, v6
	v_cndmask_b32_e32 v5, v5, v7, vcc
	v_mad_u64_u32 v[6:7], s[10:11], v4, v5, v[4:5]
	v_cmp_ne_u32_e32 vcc, v8, v6
	s_and_saveexec_b64 s[10:11], vcc
	s_xor_b64 s[10:11], exec, s[10:11]
	s_cbranch_execz .LBB0_2138
	s_add_i32 s48, s30, 0x900
	s_lshl_b64 s[12:13], s[48:49], 2
	s_add_u32 s14, s4, s12
	s_addc_u32 s15, s5, s13
	v_mov_b64_e32 v[6:7], s[14:15]
	flat_load_dword v2, v[6:7] sc1
	s_waitcnt vmcnt(0) lgkmcnt(0)
	v_cmp_eq_u32_e32 vcc, v2, v5
	s_and_saveexec_b64 s[12:13], vcc
	s_cbranch_execz .LBB0_2137
	s_mov_b32 s31, 1
	s_mov_b64 s[16:17], 0
	s_branch .LBB0_2129

.LBB0_2153:
	s_or_b64 exec, exec, s[10:11]
	s_add_i32 s48, s30, 0x900
	s_lshl_b64 s[10:11], s[48:49], 2
	s_add_u32 s4, s4, s10
	s_addc_u32 s5, s5, s11
	v_mov_b64_e32 v[4:5], s[4:5]
	s_waitcnt vmcnt(0) lgkmcnt(0)
	flat_atomic_add v[4:5], v232
	s_waitcnt vmcnt(0)

.LBB0_2279:
	s_lshl_b32 s30, s43, 6
	s_add_i32 s48, s30, 0x500
	s_lshl_b64 s[10:11], s[48:49], 2
	s_add_u32 s10, s6, s10
	s_addc_u32 s11, s7, s11
	v_mov_b64_e32 v[6:7], s[10:11]
	flat_atomic_add v6, v[6:7], v232 sc0
	v_cvt_f32_u32_e32 v5, v4
	v_sub_u32_e32 v7, 0, v4
	v_rcp_iflag_f32_e32 v5, v5
	s_nop 0
	v_mul_f32_e32 v5, 0x4f7ffffe, v5
	v_cvt_u32_f32_e32 v5, v5
	v_mul_lo_u32 v7, v7, v5
	v_mul_hi_u32 v7, v5, v7
	v_add_u32_e32 v5, v5, v7
	s_waitcnt vmcnt(0) lgkmcnt(0)
	buffer_inv sc1
	v_mul_hi_u32 v5, v6, v5
	v_mul_lo_u32 v7, v5, v4
	v_sub_u32_e32 v7, v6, v7
	v_cmp_ge_u32_e32 vcc, v7, v4
	v_add_u32_e32 v8, 1, v5
	s_nop 0
	v_cndmask_b32_e32 v5, v5, v8, vcc
	v_sub_u32_e32 v8, v7, v4
	v_cndmask_b32_e32 v7, v7, v8, vcc
	v_cmp_ge_u32_e32 vcc, v7, v4
	v_add_u32_e32 v7, 1, v5
	v_add_u32_e32 v8, 1, v6
	v_cndmask_b32_e32 v5, v5, v7, vcc
	v_mad_u64_u32 v[6:7], s[10:11], v4, v5, v[4:5]
	v_cmp_ne_u32_e32 vcc, v8, v6
	s_and_saveexec_b64 s[10:11], vcc
	s_xor_b64 s[10:11], exec, s[10:11]
	s_cbranch_execz .LBB0_2292
	s_add_i32 s48, s30, 0x900
	s_lshl_b64 s[12:13], s[48:49], 2
	s_add_u32 s14, s6, s12
	s_addc_u32 s15, s7, s13
	v_mov_b64_e32 v[6:7], s[14:15]
	flat_load_dword v2, v[6:7] sc1
	s_waitcnt vmcnt(0) lgkmcnt(0)
	v_cmp_eq_u32_e32 vcc, v2, v5
	s_and_saveexec_b64 s[12:13], vcc
	s_cbranch_execz .LBB0_2291
	s_mov_b32 s31, 1
	s_mov_b64 s[16:17], 0
	s_branch .LBB0_2283

.LBB0_2400:
	s_lshl_b32 s30, s33, 6
	s_add_i32 s48, s30, 0x500
	s_lshl_b64 s[10:11], s[48:49], 2
	s_add_u32 s10, s6, s10
	s_addc_u32 s11, s7, s11
	v_mov_b64_e32 v[6:7], s[10:11]
	flat_atomic_add v6, v[6:7], v232 sc0
	v_cvt_f32_u32_e32 v5, v4
	v_sub_u32_e32 v7, 0, v4
	v_rcp_iflag_f32_e32 v5, v5
	s_nop 0
	v_mul_f32_e32 v5, 0x4f7ffffe, v5
	v_cvt_u32_f32_e32 v5, v5
	v_mul_lo_u32 v7, v7, v5
	v_mul_hi_u32 v7, v5, v7
	v_add_u32_e32 v5, v5, v7
	s_waitcnt vmcnt(0) lgkmcnt(0)
	buffer_inv sc1
	v_mul_hi_u32 v5, v6, v5
	v_mul_lo_u32 v7, v5, v4
	v_sub_u32_e32 v7, v6, v7
	v_cmp_ge_u32_e32 vcc, v7, v4
	v_add_u32_e32 v8, 1, v5
	s_nop 0
	v_cndmask_b32_e32 v5, v5, v8, vcc
	v_sub_u32_e32 v8, v7, v4
	v_cndmask_b32_e32 v7, v7, v8, vcc
	v_cmp_ge_u32_e32 vcc, v7, v4
	v_add_u32_e32 v7, 1, v5
	v_add_u32_e32 v8, 1, v6
	v_cndmask_b32_e32 v5, v5, v7, vcc
	v_mad_u64_u32 v[6:7], s[10:11], v4, v5, v[4:5]
	v_cmp_ne_u32_e32 vcc, v8, v6
	s_and_saveexec_b64 s[10:11], vcc
	s_xor_b64 s[10:11], exec, s[10:11]
	s_cbranch_execz .LBB0_2413
	s_add_i32 s48, s30, 0x900
	s_lshl_b64 s[12:13], s[48:49], 2
	s_add_u32 s14, s6, s12
	s_addc_u32 s15, s7, s13
	v_mov_b64_e32 v[6:7], s[14:15]
	flat_load_dword v2, v[6:7] sc1
	s_waitcnt vmcnt(0) lgkmcnt(0)
	v_cmp_eq_u32_e32 vcc, v2, v5
	s_and_saveexec_b64 s[12:13], vcc
	s_cbranch_execz .LBB0_2412
	s_mov_b32 s31, 1
	s_mov_b64 s[16:17], 0
	s_branch .LBB0_2404
